# baseline (speedup 1.0000x reference)
_Z10attn64_fwdPKDF16_S0_S0_PDF16_:
	s_bfe_u32 s3, s2, 0x40003
	s_lshl_b32 s27, s3, 1
	v_readfirstlane_b32 s19, v0
	s_xor_b32 s28, s27, 31
	s_cmpk_lt_u32 s19, 0x100
	s_cselect_b64 s[4:5], -1, 0
	s_and_b64 s[4:5], s[4:5], exec
	s_cselect_b32 s29, s28, 0x63
	s_sub_i32 s8, 34, s27
	v_sub_co_u32_e64 v1, s[4:5], 3, s29
	s_and_b64 s[4:5], s[4:5], exec
	v_readfirstlane_b32 s4, v1
	s_cselect_b32 s9, 3, s4
	s_cmpk_lt_u32 s19, 0x100
	s_cselect_b64 s[4:5], -1, 0
	s_and_b64 s[4:5], s[4:5], exec
	v_sub_co_u32_e64 v1, s[6:7], 2, s29
	s_cselect_b32 s18, s9, s8
	s_sub_i32 s8, 33, s27
	s_and_b64 s[4:5], s[6:7], exec
	v_readfirstlane_b32 s4, v1
	s_cselect_b32 s6, 2, s4
	s_cmpk_lt_u32 s19, 0x100
	s_cselect_b64 s[4:5], -1, 0
	s_and_b64 s[4:5], s[4:5], exec
	s_cselect_b32 s24, s6, s8
	s_sub_i32 s4, 32, s27
	s_cmp_lg_u32 s29, 1
	s_cselect_b64 s[6:7], -1, 0
	s_cmpk_lt_u32 s19, 0x100
	v_cndmask_b32_e64 v2, 0, 1, s[6:7]
	s_cselect_b64 s[6:7], -1, 0
	s_load_dwordx8 s[8:15], s[0:1], 0x0
	s_mul_i32 s16, s28, 0x11000
	s_and_b64 s[0:1], s[6:7], exec
	s_cselect_b32 s23, 0, s16
	s_lshr_b32 s1, s2, 4
	s_and_b32 s0, s2, 7
	s_and_b32 s1, s1, 0x3fffff8
	s_or_b32 s2, s1, s0
	s_lshr_b32 s0, s19, 8
	v_mov_b32_e32 v3, s4
	s_mul_i32 s1, s0, 0xc000
	s_bfe_u32 s0, s19, 0x20006
	s_lshl_b32 s4, s2, 6
	s_lshr_b32 s2, s19, 4
	s_mov_b32 s5, 0
	v_cndmask_b32_e64 v6, v3, v2, s[6:7]
	s_lshl_b32 s3, s3, 7
	s_lshl_b32 s16, s0, 5
	v_and_b32_e32 v3, 7, v0
	s_and_b32 s2, s2, 4
	v_bfe_u32 v4, v0, 4, 2
	s_or_b32 s17, s16, s3
	s_add_i32 s22, s1, 0
	s_and_b32 s1, s19, 0x3fffffc0
	v_bitop3_b32 v4, s2, v3, v4 bitop3:0x36
	s_lshl_b64 s[2:3], s[4:5], 1
	s_waitcnt lgkmcnt(0)
	s_add_u32 s20, s12, s2
	s_addc_u32 s21, s13, s3
	s_lshl_b32 s4, s0, 10
	s_add_i32 s30, s4, s22
	v_bfe_u32 v226, v0, 3, 3
	s_cmpk_gt_u32 s19, 0xff
	v_lshl_or_b32 v2, s0, 3, v226
	s_cselect_b64 s[12:13], -1, 0
	s_xor_b32 s25, s17, 0xf80
	v_mul_u32_u24_e32 v2, 0x440, v2
	s_add_u32 s10, s10, s2
	v_lshlrev_b32_e32 v35, 1, v0
	v_lshlrev_b32_e32 v227, 3, v3
	s_addc_u32 s11, s11, s3
	v_lshlrev_b32_e32 v126, 1, v2
	v_mov_b32_e32 v127, 0
	v_bitop3_b32 v7, v35, v227, 32 bitop3:0x6c
	v_lshl_add_u64 v[2:3], s[10:11], 0, v[126:127]
	v_lshlrev_b32_e32 v4, 4, v4
	v_mov_b32_e32 v5, v127
	v_lshl_add_u64 v[222:223], v[2:3], 0, v[4:5]
	v_lshl_add_u64 v[2:3], s[20:21], 0, v[126:127]
	v_lshlrev_b32_e32 v126, 1, v7
	s_lshl_b32 s4, s23, 1
	v_lshl_add_u64 v[224:225], v[2:3], 0, v[126:127]
	v_lshl_add_u64 v[2:3], v[222:223], 0, s[4:5]
	s_mov_b32 m0, s30
	s_nop 0
	global_load_lds_dwordx4 v[2:3], off
	s_mov_b64 s[10:11], 0x11000
	v_lshl_add_u64 v[2:3], v[2:3], 0, s[10:11]
	s_add_i32 s19, s30, 0x1000
	s_mov_b32 m0, s19
	s_nop 0
	global_load_lds_dwordx4 v[2:3], off
	s_add_i32 s31, s30, 0x6000
	v_lshl_add_u64 v[2:3], v[224:225], 0, s[4:5]
	s_mov_b32 m0, s31
	s_nop 0
	global_load_lds_dwordx4 v[2:3], off
	s_add_i32 s4, s31, 0x1000
	v_lshl_add_u64 v[2:3], v[2:3], 0, s[10:11]
	s_mov_b32 m0, s4
	s_nop 0
	global_load_lds_dwordx4 v[2:3], off
	s_mov_b32 s4, 0x22000
	v_mul_lo_u32 v126, v6, s4
	s_add_i32 s4, s30, 0x2000
	v_lshl_add_u64 v[2:3], v[222:223], 0, v[126:127]
	s_mov_b32 m0, s4
	s_nop 0
	global_load_lds_dwordx4 v[2:3], off
	s_add_i32 s4, s30, 0x3000
	s_mul_i32 s23, s25, 0x440
	v_lshl_add_u64 v[2:3], v[2:3], 0, s[10:11]
	s_mov_b32 m0, s4
	s_nop 0
	global_load_lds_dwordx4 v[2:3], off
	s_lshl_b32 s4, s23, 1
	s_add_u32 s4, s8, s4
	v_and_b32_e32 v228, 31, v0
	v_bfe_u32 v1, v0, 5, 1
	s_addc_u32 s21, s9, 0
	s_add_u32 s20, s4, s2
	v_mul_u32_u24_e32 v2, 0x440, v228
	v_lshlrev_b32_e32 v233, 4, v1
	s_addc_u32 s21, s21, s3
	v_lshl_or_b32 v34, v2, 1, v233
	global_load_dwordx4 v[146:149], v34, s[20:21]
	global_load_dwordx4 v[150:153], v34, s[20:21] offset:32
	global_load_dwordx4 v[154:157], v34, s[20:21] offset:64
	global_load_dwordx4 v[158:161], v34, s[20:21] offset:96
	v_lshrrev_b32_e32 v2, 1, v0
	v_lshl_add_u32 v44, v228, 7, s22
	v_bitop3_b32 v2, v1, v2, 7 bitop3:0x78
	s_mul_i32 s20, s24, 0x11000
	v_lshl_add_u32 v234, v2, 4, v44
	v_mov_b32_e32 v2, v127
	v_mov_b32_e32 v3, v127
	v_mov_b32_e32 v4, v127
	v_mov_b32_e32 v6, v127
	v_mov_b32_e32 v7, v127
	v_mov_b32_e32 v8, v127
	v_mov_b32_e32 v9, v127
	v_mov_b32_e32 v10, v127
	v_mov_b32_e32 v11, v127
	v_mov_b32_e32 v12, v127
	v_mov_b32_e32 v13, v127
	v_mov_b32_e32 v14, v127
	v_mov_b32_e32 v15, v127
	v_mov_b32_e32 v16, v127
	v_mov_b32_e32 v17, v127
	s_ashr_i32 s21, s20, 31
	v_lshl_add_u64 v[18:19], s[20:21], 1, v[222:223]
	s_add_i32 s4, s30, 0x4000
	s_mov_b32 m0, s4
	s_nop 0
	global_load_lds_dwordx4 v[18:19], off
	v_lshl_add_u64 v[18:19], v[18:19], 0, s[10:11]
	s_add_i32 s4, s30, 0x5000
	s_mov_b32 m0, s4
	s_nop 0
	global_load_lds_dwordx4 v[18:19], off
	s_waitcnt vmcnt(6) lgkmcnt(0)
	s_barrier
	ds_read_b128 v[36:39], v234
	ds_read_b128 v[40:43], v234 offset:4096
	s_waitcnt vmcnt(5) lgkmcnt(1)
	v_mfma_f32_32x32x16_f16 v[18:33], v[36:39], v[146:149], v[2:17]
	v_bfe_u32 v45, v0, 1, 3
	v_bitop3_b32 v36, v1, v45, 2 bitop3:0x36
	v_lshl_add_u32 v235, v36, 4, v44
	v_lshlrev_b32_e32 v229, 9, v1
	s_mul_i32 s20, s18, 0x11000
	s_ashr_i32 s21, s20, 31
	s_lshl_b32 s1, s1, 2
	s_waitcnt lgkmcnt(0)
	v_mfma_f32_32x32x16_f16 v[2:17], v[40:43], v[146:149], v[2:17]
	ds_read_b128 v[36:39], v235
	ds_read_b128 v[40:43], v235 offset:4096
	s_add_i32 s24, s1, 0
	s_lshl_b32 s25, s0, 11
	s_lshl_b32 s1, s0, 13
	s_lshl_b32 s0, s0, 8
	s_add_i32 s1, s1, 0
	s_add_i32 s0, s0, 0
	s_waitcnt vmcnt(4) lgkmcnt(1)
	v_mfma_f32_32x32x16_f16 v[18:33], v[36:39], v[150:153], v[18:33]
	v_bitop3_b32 v36, v1, v45, 4 bitop3:0x36
	v_lshl_add_u32 v236, v36, 4, v44
	s_add_i32 s24, s24, 0x18000
	s_mul_i32 s26, s17, 0x440
	v_lshlrev_b32_e32 v230, 2, v1
	s_mov_b32 s38, 1
	s_movk_i32 s35, 0x2000
	s_waitcnt lgkmcnt(0)
	v_mfma_f32_32x32x16_f16 v[2:17], v[40:43], v[150:153], v[2:17]
	ds_read_b128 v[36:39], v236
	ds_read_b128 v[40:43], v236 offset:4096
	s_movk_i32 s36, 0x4000
	s_mov_b32 s34, 0x41000000
	v_or_b32_e32 v241, s16, v228
	v_or_b32_e32 v242, 0xfffff840, v230
	v_or_b32_e32 v243, 0xfffff880, v230
	v_mov_b32_e32 v244, 0x22000
	s_waitcnt vmcnt(3) lgkmcnt(1)
	v_mfma_f32_32x32x16_f16 v[18:33], v[36:39], v[154:157], v[18:33]
	v_bitop3_b32 v36, v1, v45, 6 bitop3:0x36
	v_lshl_add_u32 v237, v36, 4, v44
	v_mov_b32_e32 v245, 0xff800000
	v_mov_b32_e32 v246, v127
	v_mov_b32_e32 v247, v127
	s_waitcnt lgkmcnt(0)
	v_mfma_f32_32x32x16_f16 v[2:17], v[40:43], v[154:157], v[2:17]
	ds_read_b128 v[36:39], v237
	ds_read_b128 v[40:43], v237 offset:4096
	s_waitcnt vmcnt(2) lgkmcnt(1)
	v_mfma_f32_32x32x16_f16 v[18:33], v[36:39], v[158:161], v[18:33]
	s_waitcnt lgkmcnt(0)
	v_mfma_f32_32x32x16_f16 v[2:17], v[40:43], v[158:161], v[2:17]
	s_nop 9
	v_max_f32_e32 v36, v19, v19
	v_max_f32_e32 v37, v18, v18
	v_max_f32_e32 v36, v37, v36
	v_max3_f32 v36, v36, v2, v4
	v_max3_f32 v37, v20, v21, v3
	v_max3_f32 v36, v36, v5, v22
	v_max3_f32 v37, v37, v24, v25
	v_max3_f32 v36, v36, v23, v6
	v_max3_f32 v37, v37, v8, v9
	v_max3_f32 v36, v36, v7, v26
	v_max3_f32 v37, v37, v28, v29
	v_max3_f32 v36, v36, v27, v10
	v_max3_f32 v37, v37, v12, v13
	v_max3_f32 v36, v36, v11, v30
	v_max3_f32 v37, v37, v32, v33
	v_max3_f32 v36, v36, v31, v14
	v_max3_f32 v37, v37, v16, v17
	v_max3_f32 v36, v36, v15, v37
	v_mov_b32_e32 v37, v36
	s_nop 1
	v_permlane32_swap_b32_e32 v36, v37
	v_max_f32_e32 v37, v37, v37
	v_max_f32_e32 v36, v36, v36
	v_max_f32_e32 v248, v36, v37
	v_sub_f32_e32 v39, v3, v248
	v_lshlrev_b32_e32 v3, 5, v0
	v_sub_f32_e32 v38, v2, v248
	v_and_b32_e32 v2, 32, v35
	v_and_b32_e32 v3, 0x180, v3
	v_lshlrev_b32_e32 v35, 3, v0
	v_sub_f32_e32 v40, v4, v248
	v_add3_u32 v3, s22, v229, v3
	v_and_b32_e32 v4, 24, v35
	v_add3_u32 v50, v3, v2, v4
	v_xor_b32_e32 v2, 0x80000000, v248
	v_sub_f32_e32 v41, v5, v248
	v_sub_f32_e32 v42, v6, v248
	v_sub_f32_e32 v43, v7, v248
	v_sub_f32_e32 v44, v8, v248
	v_sub_f32_e32 v45, v9, v248
	v_sub_f32_e32 v46, v10, v248
	v_sub_f32_e32 v47, v11, v248
	v_sub_f32_e32 v48, v12, v248
	v_sub_f32_e32 v49, v13, v248
	v_sub_f32_e32 v62, v14, v248
	v_sub_f32_e32 v63, v15, v248
	v_sub_f32_e32 v64, v16, v248
	v_sub_f32_e32 v65, v17, v248
	v_mov_b32_e32 v3, v2
	v_mov_b32_e32 v4, v2
	v_mov_b32_e32 v5, v2
	v_mov_b32_e32 v6, v2
	v_mov_b32_e32 v7, v2
	v_mov_b32_e32 v8, v2
	v_mov_b32_e32 v9, v2
	v_mov_b32_e32 v10, v2
	v_mov_b32_e32 v11, v2
	v_mov_b32_e32 v12, v2
	v_mov_b32_e32 v13, v2
	v_mov_b32_e32 v14, v2
	v_mov_b32_e32 v15, v2
	v_mov_b32_e32 v16, v2
	v_mov_b32_e32 v17, v2
	s_waitcnt vmcnt(0) lgkmcnt(0)
	s_barrier
	v_sub_f32_e32 v36, v18, v248
	v_sub_f32_e32 v37, v19, v248
	v_lshl_add_u64 v[18:19], s[20:21], 1, v[222:223]
	s_mov_b32 m0, s30
	s_nop 0
	global_load_lds_dwordx4 v[18:19], off
	v_lshl_add_u64 v[18:19], v[18:19], 0, s[10:11]
	s_mov_b32 m0, s19
	s_nop 0
	global_load_lds_dwordx4 v[18:19], off
	s_add_i32 s4, s31, 0x2000
	v_lshl_add_u64 v[18:19], v[224:225], 0, v[126:127]
	s_mov_b32 m0, s4
	s_nop 0
	global_load_lds_dwordx4 v[18:19], off
	v_lshl_add_u64 v[18:19], v[18:19], 0, s[10:11]
	s_add_i32 s4, s31, 0x3000
	s_mov_b32 m0, s4
	s_nop 0
	global_load_lds_dwordx4 v[18:19], off
	ds_read_b128 v[206:209], v234 offset:8192
	ds_read_b128 v[202:205], v234 offset:12288
	ds_read_b128 v[198:201], v235 offset:8192
	ds_read_b128 v[194:197], v235 offset:12288
	ds_read_b128 v[190:193], v236 offset:8192
	ds_read_b128 v[186:189], v236 offset:12288
	ds_read_b128 v[182:185], v237 offset:8192
	ds_read_b128 v[178:181], v237 offset:12288
	s_add_i32 s4, s1, 0x18c00
	s_add_i32 s18, s0, 0x18800
	v_sub_f32_e32 v20, v20, v248
	v_sub_f32_e32 v21, v21, v248
	v_sub_f32_e32 v22, v22, v248
	v_sub_f32_e32 v23, v23, v248
	v_sub_f32_e32 v24, v24, v248
	v_sub_f32_e32 v25, v25, v248
	v_sub_f32_e32 v26, v26, v248
	v_sub_f32_e32 v27, v27, v248
	v_sub_f32_e32 v28, v28, v248
	v_sub_f32_e32 v29, v29, v248
	v_sub_f32_e32 v30, v30, v248
	v_sub_f32_e32 v31, v31, v248
	v_sub_f32_e32 v32, v32, v248
	v_sub_f32_e32 v33, v33, v248
	v_and_b32_e32 v18, 64, v35
	s_add_u32 s8, s8, s2
	v_add_u32_e32 v240, v50, v18
	v_xad_u32 v239, v18, 64, v50
	v_exp_f32_e32 v66, v36
	v_exp_f32_e32 v67, v37
	v_exp_f32_e32 v50, v38
	v_exp_f32_e32 v51, v39
	v_exp_f32_e32 v68, v20
	v_exp_f32_e32 v52, v40
	v_exp_f32_e32 v69, v21
	v_exp_f32_e32 v53, v41
	v_exp_f32_e32 v70, v22
	v_exp_f32_e32 v54, v42
	v_exp_f32_e32 v71, v23
	v_exp_f32_e32 v55, v43
	v_exp_f32_e32 v72, v24
	v_exp_f32_e32 v56, v44
	v_exp_f32_e32 v73, v25
	v_exp_f32_e32 v57, v45
	v_exp_f32_e32 v74, v26
	v_exp_f32_e32 v58, v46
	v_exp_f32_e32 v75, v27
	v_exp_f32_e32 v59, v47
	v_exp_f32_e32 v76, v28
	v_exp_f32_e32 v60, v48
	v_exp_f32_e32 v77, v29
	v_exp_f32_e32 v61, v49
	v_exp_f32_e32 v78, v30
	v_exp_f32_e32 v62, v62
	v_exp_f32_e32 v79, v31
	v_exp_f32_e32 v63, v63
	v_exp_f32_e32 v80, v32
	v_exp_f32_e32 v64, v64
	v_exp_f32_e32 v81, v33
	v_exp_f32_e32 v65, v65
	s_addc_u32 s9, s9, s3
	s_lshl_b32 s17, s26, 1
	v_and_b32_e32 v0, 63, v0
	s_waitcnt vmcnt(4) lgkmcnt(0)
	s_barrier
	s_add_u32 s8, s8, s17
	v_mov_b32_e32 v35, v127
	v_cmp_gt_u32_e64 s[0:1], 32, v0
	s_addc_u32 s9, s9, 0
	v_lshl_add_u32 v232, v0, 2, s4
	v_lshlrev_b32_e32 v0, 2, v228
	v_add_u32_e32 v231, s24, v0
	v_add_u32_e32 v238, s18, v0
	v_lshl_add_u64 v[0:1], s[8:9], 0, v[34:35]
	s_sub_i32 s33, 0, s29
	v_mov_b32_e32 v34, v127
	v_mov_b32_e32 v36, v127
	v_mov_b32_e32 v37, v127
	v_mov_b32_e32 v38, v127
	v_mov_b32_e32 v39, v127
	v_mov_b32_e32 v40, v127
	v_mov_b32_e32 v41, v127
	v_mov_b32_e32 v42, v127
	v_mov_b32_e32 v43, v127
	v_mov_b32_e32 v44, v127
	v_mov_b32_e32 v45, v127
	v_mov_b32_e32 v46, v127
	v_mov_b32_e32 v47, v127
	v_mov_b32_e32 v48, v127
	v_mov_b32_e32 v49, v127
	v_mov_b32_e32 v18, v127
	v_mov_b32_e32 v19, v127
	v_mov_b32_e32 v20, v127
	v_mov_b32_e32 v21, v127
	v_mov_b32_e32 v22, v127
	v_mov_b32_e32 v23, v127
	v_mov_b32_e32 v24, v127
	v_mov_b32_e32 v25, v127
	v_mov_b32_e32 v26, v127
	v_mov_b32_e32 v27, v127
	v_mov_b32_e32 v28, v127
	v_mov_b32_e32 v29, v127
	v_mov_b32_e32 v30, v127
	v_mov_b32_e32 v31, v127
	v_mov_b32_e32 v32, v127
	v_mov_b32_e32 v33, v127
	s_branch .LBB1_2
